# C1 + grid barriers: waiters invalidate (L1) before polling; the XCD's last arriver invalidates after the release completes and WAITS for that invalidate before it frees the waiters
# speedup vs baseline: 1.0036x; 1.0036x over previous
.LBB0_94:
	s_or_b64 exec, exec, s[8:9]
	s_mov_b64 s[8:9], exec
	v_mbcnt_lo_u32_b32 v1, s8, 0
	v_mbcnt_hi_u32_b32 v1, s9, v1
	v_cmp_eq_u32_e32 vcc, 0, v1
	s_waitcnt vmcnt(0)
	buffer_inv sc1
	s_waitcnt vmcnt(0)
	s_and_saveexec_b64 s[10:11], vcc
	s_cbranch_execz .LBB0_96
	s_bcnt1_i32_b64 s3, s[8:9]
	v_mov_b32_e32 v1, 0x2000
	v_mov_b32_e32 v2, s3
	global_atomic_add v1, v2, s[6:7] offset:1024

.LBB0_189:
	s_or_b64 exec, exec, s[10:11]
	s_mov_b64 s[10:11], exec
	v_mbcnt_lo_u32_b32 v1, s10, 0
	v_mbcnt_hi_u32_b32 v1, s11, v1
	v_cmp_eq_u32_e32 vcc, 0, v1
	s_waitcnt vmcnt(0)
	buffer_inv sc1
	s_waitcnt vmcnt(0)
	s_and_saveexec_b64 s[12:13], vcc
	s_cbranch_execz .LBB0_191
	s_bcnt1_i32_b64 s3, s[10:11]
	v_mov_b32_e32 v1, 0x2000
	v_mov_b32_e32 v2, s3
	global_atomic_add v1, v2, s[8:9] offset:1024

.LBB0_643:
	s_or_b64 exec, exec, s[8:9]
	s_mov_b64 s[8:9], exec
	v_mbcnt_lo_u32_b32 v1, s8, 0
	v_mbcnt_hi_u32_b32 v1, s9, v1
	v_cmp_eq_u32_e32 vcc, 0, v1
	s_waitcnt vmcnt(0)
	buffer_inv sc1
	s_waitcnt vmcnt(0)
	s_and_saveexec_b64 s[10:11], vcc
	s_cbranch_execz .LBB0_645
	s_bcnt1_i32_b64 s2, s[8:9]
	v_mov_b32_e32 v1, 0x2000
	v_mov_b32_e32 v2, s2
	global_atomic_add v1, v2, s[6:7] offset:1024

.LBB0_1195:
	s_or_b64 exec, exec, s[8:9]
	s_mov_b64 s[8:9], exec
	v_mbcnt_lo_u32_b32 v1, s8, 0
	v_mbcnt_hi_u32_b32 v1, s9, v1
	v_cmp_eq_u32_e32 vcc, 0, v1
	s_waitcnt vmcnt(0)
	buffer_inv sc1
	s_waitcnt vmcnt(0)
	s_and_saveexec_b64 s[10:11], vcc
	s_cbranch_execz .LBB0_1197
	s_bcnt1_i32_b64 s2, s[8:9]
	v_mov_b32_e32 v1, 0x2000
	v_mov_b32_e32 v2, s2
	global_atomic_add v1, v2, s[4:5] offset:1024

.LBB0_1294:
	s_or_b64 exec, exec, s[10:11]
	s_mov_b64 s[10:11], exec
	v_mbcnt_lo_u32_b32 v1, s10, 0
	v_mbcnt_hi_u32_b32 v1, s11, v1
	v_cmp_eq_u32_e32 vcc, 0, v1
	s_waitcnt vmcnt(0)
	buffer_inv sc1
	s_waitcnt vmcnt(0)
	s_and_saveexec_b64 s[12:13], vcc
	s_cbranch_execz .LBB0_1296
	s_bcnt1_i32_b64 s2, s[10:11]
	v_mov_b32_e32 v1, 0x2000
	v_mov_b32_e32 v2, s2
	global_atomic_add v1, v2, s[8:9] offset:1024

.LBB0_1463:
	s_or_b64 exec, exec, s[18:19]
	s_mov_b64 s[18:19], exec
	v_mbcnt_lo_u32_b32 v1, s18, 0
	v_mbcnt_hi_u32_b32 v1, s19, v1
	v_cmp_eq_u32_e32 vcc, 0, v1
	s_waitcnt vmcnt(0)
	buffer_inv sc1
	s_waitcnt vmcnt(0)
	s_and_saveexec_b64 s[30:31], vcc
	s_cbranch_execz .LBB0_1465
	s_bcnt1_i32_b64 s2, s[18:19]
	v_mov_b32_e32 v1, 0x2000
	v_mov_b32_e32 v2, s2
	global_atomic_add v1, v2, s[10:11] offset:1024

.LBB0_1713:
	s_or_b64 exec, exec, s[6:7]
	s_mov_b64 s[6:7], exec
	v_mbcnt_lo_u32_b32 v0, s6, 0
	v_mbcnt_hi_u32_b32 v0, s7, v0
	v_cmp_eq_u32_e32 vcc, 0, v0
	s_waitcnt vmcnt(0)
	buffer_inv sc1
	s_waitcnt vmcnt(0)
	s_and_saveexec_b64 s[8:9], vcc
	s_cbranch_execz .LBB0_1715
	s_bcnt1_i32_b64 s6, s[6:7]
	v_mov_b32_e32 v0, 0x2000
	v_mov_b32_e32 v1, s6
	global_atomic_add v0, v1, s[4:5] offset:1024
